# P0 fold on v_mfma_f32_16x16x4_f32 (f32 operands), fold staging and the w_in / w_out transpose items with all loads in flight
# speedup vs baseline: 1.0104x; 1.0104x over previous
.LBB0_30:
	s_barrier
	s_and_saveexec_b64 s[18:19], s[4:5]
	ds_write2st64_b32 v1, v27, v7 offset0:129 offset1:131
	s_or_b64 exec, exec, s[18:19]
	s_lshl_b32 s18, s62, 3
	s_and_b32 s43, s62, 7
	s_and_b32 s42, s18, 0xffffffc0
	s_and_saveexec_b64 s[44:45], s[6:7]
	s_cbranch_execz .LBB0_44
	s_mul_i32 s18, s42, 0x3000
	s_lshl_b32 s19, s43, 9
	s_add_i32 s18, s18, s19
	s_add_i32 s18, s18, 0x2000
	v_ashrrev_i32_e32 v10, 7, v38
	v_mul_u32_u24_e32 v11, 0x3000, v10
	v_mul_u32_u24_e32 v12, 0x204, v10
	v_add3_u32 v146, v11, v4, s18
	v_add_u32_e32 v162, v12, v6
	v_add_u32_e32 v147, 0xc000, v146
	v_add_u32_e32 v148, 0x18000, v146
	v_add_u32_e32 v149, 0x24000, v146
	v_add_u32_e32 v150, 0x30000, v146
	v_add_u32_e32 v151, 0x3c000, v146
	v_add_u32_e32 v152, 0x48000, v146
	v_add_u32_e32 v153, 0x54000, v146
	v_add_u32_e32 v154, 0x60000, v146
	v_add_u32_e32 v155, 0x6c000, v146
	v_add_u32_e32 v156, 0x78000, v146
	v_add_u32_e32 v157, 0x84000, v146
	v_add_u32_e32 v158, 0x90000, v146
	v_add_u32_e32 v159, 0x9c000, v146
	v_add_u32_e32 v160, 0xa8000, v146
	v_add_u32_e32 v161, 0xb4000, v146
	global_load_dword v130, v146, s[22:23]
	global_load_dword v131, v147, s[22:23]
	global_load_dword v132, v148, s[22:23]
	global_load_dword v133, v149, s[22:23]
	global_load_dword v134, v150, s[22:23]
	global_load_dword v135, v151, s[22:23]
	global_load_dword v136, v152, s[22:23]
	global_load_dword v137, v153, s[22:23]
	global_load_dword v138, v154, s[22:23]
	global_load_dword v139, v155, s[22:23]
	global_load_dword v140, v156, s[22:23]
	global_load_dword v141, v157, s[22:23]
	global_load_dword v142, v158, s[22:23]
	global_load_dword v143, v159, s[22:23]
	global_load_dword v144, v160, s[22:23]
	global_load_dword v145, v161, s[22:23]
	s_waitcnt vmcnt(15)
	ds_write_b32 v162, v130
	s_waitcnt vmcnt(14)
	ds_write_b32 v162, v131 offset:2064
	s_waitcnt vmcnt(13)
	ds_write_b32 v162, v132 offset:4128
	s_waitcnt vmcnt(12)
	ds_write_b32 v162, v133 offset:6192
	s_waitcnt vmcnt(11)
	ds_write_b32 v162, v134 offset:8256
	s_waitcnt vmcnt(10)
	ds_write_b32 v162, v135 offset:10320
	s_waitcnt vmcnt(9)
	ds_write_b32 v162, v136 offset:12384
	s_waitcnt vmcnt(8)
	ds_write_b32 v162, v137 offset:14448
	s_waitcnt vmcnt(7)
	ds_write_b32 v162, v138 offset:16512
	s_waitcnt vmcnt(6)
	ds_write_b32 v162, v139 offset:18576
	s_waitcnt vmcnt(5)
	ds_write_b32 v162, v140 offset:20640
	s_waitcnt vmcnt(4)
	ds_write_b32 v162, v141 offset:22704
	s_waitcnt vmcnt(3)
	ds_write_b32 v162, v142 offset:24768
	s_waitcnt vmcnt(2)
	ds_write_b32 v162, v143 offset:26832
	s_waitcnt vmcnt(1)
	ds_write_b32 v162, v144 offset:28896
	s_waitcnt vmcnt(0)
	ds_write_b32 v162, v145 offset:30960
.LBB0_44:
	s_or_b64 exec, exec, s[44:45]
	v_and_b32_e32 v110, 63, v38
	v_and_b32_e32 v111, 15, v110
	v_lshrrev_b32_e32 v112, 4, v110
	s_lshl_b32 s18, s76, 4
	v_add_u32_e32 v113, s18, v111
	v_cmp_gt_u32_e32 vcc, 0x41, v113
	v_subrev_u32_e32 v114, 64, v113
	v_mov_b32_e32 v115, 0x8300
	v_mov_b32_e32 v116, 0x8100
	v_bfrev_b32_e32 v117, 1
	v_mov_b32_e32 v118, 0
	v_cndmask_b32_e32 v114, v114, v113, vcc
	v_cndmask_b32_e32 v115, v115, v116, vcc
	v_cndmask_b32_e32 v117, v117, v118, vcc
	v_mul_u32_u24_e32 v116, v112, v114
	v_lshlrev_b32_e32 v119, 2, v114
	v_mul_u32_u24_e32 v120, 0x204, v111
	v_lshl_add_u32 v120, v112, 2, v120
	s_waitcnt lgkmcnt(0)
	s_barrier
	v_and_b32_e32 v121, 0x7f, v116
	v_add_u32_e32 v116, v116, v119
	v_lshl_add_u32 v121, v121, 2, v115
	ds_read_b32 v156, v121
	ds_read_b32 v132, v120
	ds_read_b32 v133, v120 offset:8256
	ds_read_b32 v134, v120 offset:16512
	ds_read_b32 v135, v120 offset:24768
	v_and_b32_e32 v121, 0x7f, v116
	v_add_u32_e32 v116, v116, v119
	v_lshl_add_u32 v121, v121, 2, v115
	ds_read_b32 v157, v121
	ds_read_b32 v136, v120 offset:16
	ds_read_b32 v137, v120 offset:8272
	ds_read_b32 v138, v120 offset:16528
	ds_read_b32 v139, v120 offset:24784
	v_and_b32_e32 v121, 0x7f, v116
	v_add_u32_e32 v116, v116, v119
	v_lshl_add_u32 v121, v121, 2, v115
	ds_read_b32 v160, v121
	ds_read_b32 v140, v120 offset:32
	ds_read_b32 v141, v120 offset:8288
	ds_read_b32 v142, v120 offset:16544
	ds_read_b32 v143, v120 offset:24800
	v_and_b32_e32 v121, 0x7f, v116
	v_add_u32_e32 v116, v116, v119
	v_lshl_add_u32 v121, v121, 2, v115
	ds_read_b32 v161, v121
	ds_read_b32 v144, v120 offset:48
	ds_read_b32 v145, v120 offset:8304
	ds_read_b32 v146, v120 offset:16560
	ds_read_b32 v147, v120 offset:24816
	s_waitcnt lgkmcnt(10)
	v_xor_b32_e32 v156, v117, v156
	v_xor_b32_e32 v157, v117, v157
	s_nop 1
	v_mfma_f32_16x16x4_f32 v[164:167], v132, v156, 0
	v_mfma_f32_16x16x4_f32 v[168:171], v133, v156, 0
	v_mfma_f32_16x16x4_f32 v[172:175], v134, v156, 0
	v_mfma_f32_16x16x4_f32 v[176:179], v135, v156, 0
	v_mfma_f32_16x16x4_f32 v[164:167], v136, v157, v[164:167]
	v_mfma_f32_16x16x4_f32 v[168:171], v137, v157, v[168:171]
	v_mfma_f32_16x16x4_f32 v[172:175], v138, v157, v[172:175]
	v_mfma_f32_16x16x4_f32 v[176:179], v139, v157, v[176:179]
	v_and_b32_e32 v121, 0x7f, v116
	v_add_u32_e32 v116, v116, v119
	v_lshl_add_u32 v121, v121, 2, v115
	ds_read_b32 v156, v121
	ds_read_b32 v132, v120 offset:64
	ds_read_b32 v133, v120 offset:8320
	ds_read_b32 v134, v120 offset:16576
	ds_read_b32 v135, v120 offset:24832
	v_and_b32_e32 v121, 0x7f, v116
	v_add_u32_e32 v116, v116, v119
	v_lshl_add_u32 v121, v121, 2, v115
	ds_read_b32 v157, v121
	ds_read_b32 v136, v120 offset:80
	ds_read_b32 v137, v120 offset:8336
	ds_read_b32 v138, v120 offset:16592
	ds_read_b32 v139, v120 offset:24848
	s_waitcnt lgkmcnt(10)
	v_xor_b32_e32 v160, v117, v160
	v_xor_b32_e32 v161, v117, v161
	s_nop 1
	v_mfma_f32_16x16x4_f32 v[164:167], v140, v160, v[164:167]
	v_mfma_f32_16x16x4_f32 v[168:171], v141, v160, v[168:171]
	v_mfma_f32_16x16x4_f32 v[172:175], v142, v160, v[172:175]
	v_mfma_f32_16x16x4_f32 v[176:179], v143, v160, v[176:179]
	v_mfma_f32_16x16x4_f32 v[164:167], v144, v161, v[164:167]
	v_mfma_f32_16x16x4_f32 v[168:171], v145, v161, v[168:171]
	v_mfma_f32_16x16x4_f32 v[172:175], v146, v161, v[172:175]
	v_mfma_f32_16x16x4_f32 v[176:179], v147, v161, v[176:179]
	v_and_b32_e32 v121, 0x7f, v116
	v_add_u32_e32 v116, v116, v119
	v_lshl_add_u32 v121, v121, 2, v115
	ds_read_b32 v160, v121
	ds_read_b32 v140, v120 offset:96
	ds_read_b32 v141, v120 offset:8352
	ds_read_b32 v142, v120 offset:16608
	ds_read_b32 v143, v120 offset:24864
	v_and_b32_e32 v121, 0x7f, v116
	v_add_u32_e32 v116, v116, v119
	v_lshl_add_u32 v121, v121, 2, v115
	ds_read_b32 v161, v121
	ds_read_b32 v144, v120 offset:112
	ds_read_b32 v145, v120 offset:8368
	ds_read_b32 v146, v120 offset:16624
	ds_read_b32 v147, v120 offset:24880
	s_waitcnt lgkmcnt(10)
	v_xor_b32_e32 v156, v117, v156
	v_xor_b32_e32 v157, v117, v157
	s_nop 1
	v_mfma_f32_16x16x4_f32 v[164:167], v132, v156, v[164:167]
	v_mfma_f32_16x16x4_f32 v[168:171], v133, v156, v[168:171]
	v_mfma_f32_16x16x4_f32 v[172:175], v134, v156, v[172:175]
	v_mfma_f32_16x16x4_f32 v[176:179], v135, v156, v[176:179]
	v_mfma_f32_16x16x4_f32 v[164:167], v136, v157, v[164:167]
	v_mfma_f32_16x16x4_f32 v[168:171], v137, v157, v[168:171]
	v_mfma_f32_16x16x4_f32 v[172:175], v138, v157, v[172:175]
	v_mfma_f32_16x16x4_f32 v[176:179], v139, v157, v[176:179]
	v_and_b32_e32 v121, 0x7f, v116
	v_add_u32_e32 v116, v116, v119
	v_lshl_add_u32 v121, v121, 2, v115
	ds_read_b32 v156, v121
	ds_read_b32 v132, v120 offset:128
	ds_read_b32 v133, v120 offset:8384
	ds_read_b32 v134, v120 offset:16640
	ds_read_b32 v135, v120 offset:24896
	v_and_b32_e32 v121, 0x7f, v116
	v_add_u32_e32 v116, v116, v119
	v_lshl_add_u32 v121, v121, 2, v115
	ds_read_b32 v157, v121
	ds_read_b32 v136, v120 offset:144
	ds_read_b32 v137, v120 offset:8400
	ds_read_b32 v138, v120 offset:16656
	ds_read_b32 v139, v120 offset:24912
	s_waitcnt lgkmcnt(10)
	v_xor_b32_e32 v160, v117, v160
	v_xor_b32_e32 v161, v117, v161
	s_nop 1
	v_mfma_f32_16x16x4_f32 v[164:167], v140, v160, v[164:167]
	v_mfma_f32_16x16x4_f32 v[168:171], v141, v160, v[168:171]
	v_mfma_f32_16x16x4_f32 v[172:175], v142, v160, v[172:175]
	v_mfma_f32_16x16x4_f32 v[176:179], v143, v160, v[176:179]
	v_mfma_f32_16x16x4_f32 v[164:167], v144, v161, v[164:167]
	v_mfma_f32_16x16x4_f32 v[168:171], v145, v161, v[168:171]
	v_mfma_f32_16x16x4_f32 v[172:175], v146, v161, v[172:175]
	v_mfma_f32_16x16x4_f32 v[176:179], v147, v161, v[176:179]
	v_and_b32_e32 v121, 0x7f, v116
	v_add_u32_e32 v116, v116, v119
	v_lshl_add_u32 v121, v121, 2, v115
	ds_read_b32 v160, v121
	ds_read_b32 v140, v120 offset:160
	ds_read_b32 v141, v120 offset:8416
	ds_read_b32 v142, v120 offset:16672
	ds_read_b32 v143, v120 offset:24928
	v_and_b32_e32 v121, 0x7f, v116
	v_add_u32_e32 v116, v116, v119
	v_lshl_add_u32 v121, v121, 2, v115
	ds_read_b32 v161, v121
	ds_read_b32 v144, v120 offset:176
	ds_read_b32 v145, v120 offset:8432
	ds_read_b32 v146, v120 offset:16688
	ds_read_b32 v147, v120 offset:24944
	s_waitcnt lgkmcnt(10)
	v_xor_b32_e32 v156, v117, v156
	v_xor_b32_e32 v157, v117, v157
	s_nop 1
	v_mfma_f32_16x16x4_f32 v[164:167], v132, v156, v[164:167]
	v_mfma_f32_16x16x4_f32 v[168:171], v133, v156, v[168:171]
	v_mfma_f32_16x16x4_f32 v[172:175], v134, v156, v[172:175]
	v_mfma_f32_16x16x4_f32 v[176:179], v135, v156, v[176:179]
	v_mfma_f32_16x16x4_f32 v[164:167], v136, v157, v[164:167]
	v_mfma_f32_16x16x4_f32 v[168:171], v137, v157, v[168:171]
	v_mfma_f32_16x16x4_f32 v[172:175], v138, v157, v[172:175]
	v_mfma_f32_16x16x4_f32 v[176:179], v139, v157, v[176:179]
	v_and_b32_e32 v121, 0x7f, v116
	v_add_u32_e32 v116, v116, v119
	v_lshl_add_u32 v121, v121, 2, v115
	ds_read_b32 v156, v121
	ds_read_b32 v132, v120 offset:192
	ds_read_b32 v133, v120 offset:8448
	ds_read_b32 v134, v120 offset:16704
	ds_read_b32 v135, v120 offset:24960
	v_and_b32_e32 v121, 0x7f, v116
	v_add_u32_e32 v116, v116, v119
	v_lshl_add_u32 v121, v121, 2, v115
	ds_read_b32 v157, v121
	ds_read_b32 v136, v120 offset:208
	ds_read_b32 v137, v120 offset:8464
	ds_read_b32 v138, v120 offset:16720
	ds_read_b32 v139, v120 offset:24976
	s_waitcnt lgkmcnt(10)
	v_xor_b32_e32 v160, v117, v160
	v_xor_b32_e32 v161, v117, v161
	s_nop 1
	v_mfma_f32_16x16x4_f32 v[164:167], v140, v160, v[164:167]
	v_mfma_f32_16x16x4_f32 v[168:171], v141, v160, v[168:171]
	v_mfma_f32_16x16x4_f32 v[172:175], v142, v160, v[172:175]
	v_mfma_f32_16x16x4_f32 v[176:179], v143, v160, v[176:179]
	v_mfma_f32_16x16x4_f32 v[164:167], v144, v161, v[164:167]
	v_mfma_f32_16x16x4_f32 v[168:171], v145, v161, v[168:171]
	v_mfma_f32_16x16x4_f32 v[172:175], v146, v161, v[172:175]
	v_mfma_f32_16x16x4_f32 v[176:179], v147, v161, v[176:179]
	v_and_b32_e32 v121, 0x7f, v116
	v_add_u32_e32 v116, v116, v119
	v_lshl_add_u32 v121, v121, 2, v115
	ds_read_b32 v160, v121
	ds_read_b32 v140, v120 offset:224
	ds_read_b32 v141, v120 offset:8480
	ds_read_b32 v142, v120 offset:16736
	ds_read_b32 v143, v120 offset:24992
	v_and_b32_e32 v121, 0x7f, v116
	v_add_u32_e32 v116, v116, v119
	v_lshl_add_u32 v121, v121, 2, v115
	ds_read_b32 v161, v121
	ds_read_b32 v144, v120 offset:240
	ds_read_b32 v145, v120 offset:8496
	ds_read_b32 v146, v120 offset:16752
	ds_read_b32 v147, v120 offset:25008
	s_waitcnt lgkmcnt(10)
	v_xor_b32_e32 v156, v117, v156
	v_xor_b32_e32 v157, v117, v157
	s_nop 1
	v_mfma_f32_16x16x4_f32 v[164:167], v132, v156, v[164:167]
	v_mfma_f32_16x16x4_f32 v[168:171], v133, v156, v[168:171]
	v_mfma_f32_16x16x4_f32 v[172:175], v134, v156, v[172:175]
	v_mfma_f32_16x16x4_f32 v[176:179], v135, v156, v[176:179]
	v_mfma_f32_16x16x4_f32 v[164:167], v136, v157, v[164:167]
	v_mfma_f32_16x16x4_f32 v[168:171], v137, v157, v[168:171]
	v_mfma_f32_16x16x4_f32 v[172:175], v138, v157, v[172:175]
	v_mfma_f32_16x16x4_f32 v[176:179], v139, v157, v[176:179]
	v_and_b32_e32 v121, 0x7f, v116
	v_add_u32_e32 v116, v116, v119
	v_lshl_add_u32 v121, v121, 2, v115
	ds_read_b32 v156, v121
	ds_read_b32 v132, v120 offset:256
	ds_read_b32 v133, v120 offset:8512
	ds_read_b32 v134, v120 offset:16768
	ds_read_b32 v135, v120 offset:25024
	v_and_b32_e32 v121, 0x7f, v116
	v_add_u32_e32 v116, v116, v119
	v_lshl_add_u32 v121, v121, 2, v115
	ds_read_b32 v157, v121
	ds_read_b32 v136, v120 offset:272
	ds_read_b32 v137, v120 offset:8528
	ds_read_b32 v138, v120 offset:16784
	ds_read_b32 v139, v120 offset:25040
	s_waitcnt lgkmcnt(10)
	v_xor_b32_e32 v160, v117, v160
	v_xor_b32_e32 v161, v117, v161
	s_nop 1
	v_mfma_f32_16x16x4_f32 v[164:167], v140, v160, v[164:167]
	v_mfma_f32_16x16x4_f32 v[168:171], v141, v160, v[168:171]
	v_mfma_f32_16x16x4_f32 v[172:175], v142, v160, v[172:175]
	v_mfma_f32_16x16x4_f32 v[176:179], v143, v160, v[176:179]
	v_mfma_f32_16x16x4_f32 v[164:167], v144, v161, v[164:167]
	v_mfma_f32_16x16x4_f32 v[168:171], v145, v161, v[168:171]
	v_mfma_f32_16x16x4_f32 v[172:175], v146, v161, v[172:175]
	v_mfma_f32_16x16x4_f32 v[176:179], v147, v161, v[176:179]
	v_and_b32_e32 v121, 0x7f, v116
	v_add_u32_e32 v116, v116, v119
	v_lshl_add_u32 v121, v121, 2, v115
	ds_read_b32 v160, v121
	ds_read_b32 v140, v120 offset:288
	ds_read_b32 v141, v120 offset:8544
	ds_read_b32 v142, v120 offset:16800
	ds_read_b32 v143, v120 offset:25056
	v_and_b32_e32 v121, 0x7f, v116
	v_add_u32_e32 v116, v116, v119
	v_lshl_add_u32 v121, v121, 2, v115
	ds_read_b32 v161, v121
	ds_read_b32 v144, v120 offset:304
	ds_read_b32 v145, v120 offset:8560
	ds_read_b32 v146, v120 offset:16816
	ds_read_b32 v147, v120 offset:25072
	s_waitcnt lgkmcnt(10)
	v_xor_b32_e32 v156, v117, v156
	v_xor_b32_e32 v157, v117, v157
	s_nop 1
	v_mfma_f32_16x16x4_f32 v[164:167], v132, v156, v[164:167]
	v_mfma_f32_16x16x4_f32 v[168:171], v133, v156, v[168:171]
	v_mfma_f32_16x16x4_f32 v[172:175], v134, v156, v[172:175]
	v_mfma_f32_16x16x4_f32 v[176:179], v135, v156, v[176:179]
	v_mfma_f32_16x16x4_f32 v[164:167], v136, v157, v[164:167]
	v_mfma_f32_16x16x4_f32 v[168:171], v137, v157, v[168:171]
	v_mfma_f32_16x16x4_f32 v[172:175], v138, v157, v[172:175]
	v_mfma_f32_16x16x4_f32 v[176:179], v139, v157, v[176:179]
	v_and_b32_e32 v121, 0x7f, v116
	v_add_u32_e32 v116, v116, v119
	v_lshl_add_u32 v121, v121, 2, v115
	ds_read_b32 v156, v121
	ds_read_b32 v132, v120 offset:320
	ds_read_b32 v133, v120 offset:8576
	ds_read_b32 v134, v120 offset:16832
	ds_read_b32 v135, v120 offset:25088
	v_and_b32_e32 v121, 0x7f, v116
	v_add_u32_e32 v116, v116, v119
	v_lshl_add_u32 v121, v121, 2, v115
	ds_read_b32 v157, v121
	ds_read_b32 v136, v120 offset:336
	ds_read_b32 v137, v120 offset:8592
	ds_read_b32 v138, v120 offset:16848
	ds_read_b32 v139, v120 offset:25104
	s_waitcnt lgkmcnt(10)
	v_xor_b32_e32 v160, v117, v160
	v_xor_b32_e32 v161, v117, v161
	s_nop 1
	v_mfma_f32_16x16x4_f32 v[164:167], v140, v160, v[164:167]
	v_mfma_f32_16x16x4_f32 v[168:171], v141, v160, v[168:171]
	v_mfma_f32_16x16x4_f32 v[172:175], v142, v160, v[172:175]
	v_mfma_f32_16x16x4_f32 v[176:179], v143, v160, v[176:179]
	v_mfma_f32_16x16x4_f32 v[164:167], v144, v161, v[164:167]
	v_mfma_f32_16x16x4_f32 v[168:171], v145, v161, v[168:171]
	v_mfma_f32_16x16x4_f32 v[172:175], v146, v161, v[172:175]
	v_mfma_f32_16x16x4_f32 v[176:179], v147, v161, v[176:179]
	v_and_b32_e32 v121, 0x7f, v116
	v_add_u32_e32 v116, v116, v119
	v_lshl_add_u32 v121, v121, 2, v115
	ds_read_b32 v160, v121
	ds_read_b32 v140, v120 offset:352
	ds_read_b32 v141, v120 offset:8608
	ds_read_b32 v142, v120 offset:16864
	ds_read_b32 v143, v120 offset:25120
	v_and_b32_e32 v121, 0x7f, v116
	v_add_u32_e32 v116, v116, v119
	v_lshl_add_u32 v121, v121, 2, v115
	ds_read_b32 v161, v121
	ds_read_b32 v144, v120 offset:368
	ds_read_b32 v145, v120 offset:8624
	ds_read_b32 v146, v120 offset:16880
	ds_read_b32 v147, v120 offset:25136
	s_waitcnt lgkmcnt(10)
	v_xor_b32_e32 v156, v117, v156
	v_xor_b32_e32 v157, v117, v157
	s_nop 1
	v_mfma_f32_16x16x4_f32 v[164:167], v132, v156, v[164:167]
	v_mfma_f32_16x16x4_f32 v[168:171], v133, v156, v[168:171]
	v_mfma_f32_16x16x4_f32 v[172:175], v134, v156, v[172:175]
	v_mfma_f32_16x16x4_f32 v[176:179], v135, v156, v[176:179]
	v_mfma_f32_16x16x4_f32 v[164:167], v136, v157, v[164:167]
	v_mfma_f32_16x16x4_f32 v[168:171], v137, v157, v[168:171]
	v_mfma_f32_16x16x4_f32 v[172:175], v138, v157, v[172:175]
	v_mfma_f32_16x16x4_f32 v[176:179], v139, v157, v[176:179]
	v_and_b32_e32 v121, 0x7f, v116
	v_add_u32_e32 v116, v116, v119
	v_lshl_add_u32 v121, v121, 2, v115
	ds_read_b32 v156, v121
	ds_read_b32 v132, v120 offset:384
	ds_read_b32 v133, v120 offset:8640
	ds_read_b32 v134, v120 offset:16896
	ds_read_b32 v135, v120 offset:25152
	v_and_b32_e32 v121, 0x7f, v116
	v_add_u32_e32 v116, v116, v119
	v_lshl_add_u32 v121, v121, 2, v115
	ds_read_b32 v157, v121
	ds_read_b32 v136, v120 offset:400
	ds_read_b32 v137, v120 offset:8656
	ds_read_b32 v138, v120 offset:16912
	ds_read_b32 v139, v120 offset:25168
	s_waitcnt lgkmcnt(10)
	v_xor_b32_e32 v160, v117, v160
	v_xor_b32_e32 v161, v117, v161
	s_nop 1
	v_mfma_f32_16x16x4_f32 v[164:167], v140, v160, v[164:167]
	v_mfma_f32_16x16x4_f32 v[168:171], v141, v160, v[168:171]
	v_mfma_f32_16x16x4_f32 v[172:175], v142, v160, v[172:175]
	v_mfma_f32_16x16x4_f32 v[176:179], v143, v160, v[176:179]
	v_mfma_f32_16x16x4_f32 v[164:167], v144, v161, v[164:167]
	v_mfma_f32_16x16x4_f32 v[168:171], v145, v161, v[168:171]
	v_mfma_f32_16x16x4_f32 v[172:175], v146, v161, v[172:175]
	v_mfma_f32_16x16x4_f32 v[176:179], v147, v161, v[176:179]
	v_and_b32_e32 v121, 0x7f, v116
	v_add_u32_e32 v116, v116, v119
	v_lshl_add_u32 v121, v121, 2, v115
	ds_read_b32 v160, v121
	ds_read_b32 v140, v120 offset:416
	ds_read_b32 v141, v120 offset:8672
	ds_read_b32 v142, v120 offset:16928
	ds_read_b32 v143, v120 offset:25184
	v_and_b32_e32 v121, 0x7f, v116
	v_add_u32_e32 v116, v116, v119
	v_lshl_add_u32 v121, v121, 2, v115
	ds_read_b32 v161, v121
	ds_read_b32 v144, v120 offset:432
	ds_read_b32 v145, v120 offset:8688
	ds_read_b32 v146, v120 offset:16944
	ds_read_b32 v147, v120 offset:25200
	s_waitcnt lgkmcnt(10)
	v_xor_b32_e32 v156, v117, v156
	v_xor_b32_e32 v157, v117, v157
	s_nop 1
	v_mfma_f32_16x16x4_f32 v[164:167], v132, v156, v[164:167]
	v_mfma_f32_16x16x4_f32 v[168:171], v133, v156, v[168:171]
	v_mfma_f32_16x16x4_f32 v[172:175], v134, v156, v[172:175]
	v_mfma_f32_16x16x4_f32 v[176:179], v135, v156, v[176:179]
	v_mfma_f32_16x16x4_f32 v[164:167], v136, v157, v[164:167]
	v_mfma_f32_16x16x4_f32 v[168:171], v137, v157, v[168:171]
	v_mfma_f32_16x16x4_f32 v[172:175], v138, v157, v[172:175]
	v_mfma_f32_16x16x4_f32 v[176:179], v139, v157, v[176:179]
	v_and_b32_e32 v121, 0x7f, v116
	v_add_u32_e32 v116, v116, v119
	v_lshl_add_u32 v121, v121, 2, v115
	ds_read_b32 v156, v121
	ds_read_b32 v132, v120 offset:448
	ds_read_b32 v133, v120 offset:8704
	ds_read_b32 v134, v120 offset:16960
	ds_read_b32 v135, v120 offset:25216
	v_and_b32_e32 v121, 0x7f, v116
	v_add_u32_e32 v116, v116, v119
	v_lshl_add_u32 v121, v121, 2, v115
	ds_read_b32 v157, v121
	ds_read_b32 v136, v120 offset:464
	ds_read_b32 v137, v120 offset:8720
	ds_read_b32 v138, v120 offset:16976
	ds_read_b32 v139, v120 offset:25232
	s_waitcnt lgkmcnt(10)
	v_xor_b32_e32 v160, v117, v160
	v_xor_b32_e32 v161, v117, v161
	s_nop 1
	v_mfma_f32_16x16x4_f32 v[164:167], v140, v160, v[164:167]
	v_mfma_f32_16x16x4_f32 v[168:171], v141, v160, v[168:171]
	v_mfma_f32_16x16x4_f32 v[172:175], v142, v160, v[172:175]
	v_mfma_f32_16x16x4_f32 v[176:179], v143, v160, v[176:179]
	v_mfma_f32_16x16x4_f32 v[164:167], v144, v161, v[164:167]
	v_mfma_f32_16x16x4_f32 v[168:171], v145, v161, v[168:171]
	v_mfma_f32_16x16x4_f32 v[172:175], v146, v161, v[172:175]
	v_mfma_f32_16x16x4_f32 v[176:179], v147, v161, v[176:179]
	v_and_b32_e32 v121, 0x7f, v116
	v_add_u32_e32 v116, v116, v119
	v_lshl_add_u32 v121, v121, 2, v115
	ds_read_b32 v160, v121
	ds_read_b32 v140, v120 offset:480
	ds_read_b32 v141, v120 offset:8736
	ds_read_b32 v142, v120 offset:16992
	ds_read_b32 v143, v120 offset:25248
	v_and_b32_e32 v121, 0x7f, v116
	v_add_u32_e32 v116, v116, v119
	v_lshl_add_u32 v121, v121, 2, v115
	ds_read_b32 v161, v121
	ds_read_b32 v144, v120 offset:496
	ds_read_b32 v145, v120 offset:8752
	ds_read_b32 v146, v120 offset:17008
	ds_read_b32 v147, v120 offset:25264
	s_waitcnt lgkmcnt(10)
	v_xor_b32_e32 v156, v117, v156
	v_xor_b32_e32 v157, v117, v157
	s_nop 1
	v_mfma_f32_16x16x4_f32 v[164:167], v132, v156, v[164:167]
	v_mfma_f32_16x16x4_f32 v[168:171], v133, v156, v[168:171]
	v_mfma_f32_16x16x4_f32 v[172:175], v134, v156, v[172:175]
	v_mfma_f32_16x16x4_f32 v[176:179], v135, v156, v[176:179]
	v_mfma_f32_16x16x4_f32 v[164:167], v136, v157, v[164:167]
	v_mfma_f32_16x16x4_f32 v[168:171], v137, v157, v[168:171]
	v_mfma_f32_16x16x4_f32 v[172:175], v138, v157, v[172:175]
	v_mfma_f32_16x16x4_f32 v[176:179], v139, v157, v[176:179]
	s_waitcnt lgkmcnt(0)
	v_xor_b32_e32 v160, v117, v160
	v_xor_b32_e32 v161, v117, v161
	s_nop 1
	v_mfma_f32_16x16x4_f32 v[164:167], v140, v160, v[164:167]
	v_mfma_f32_16x16x4_f32 v[168:171], v141, v160, v[168:171]
	v_mfma_f32_16x16x4_f32 v[172:175], v142, v160, v[172:175]
	v_mfma_f32_16x16x4_f32 v[176:179], v143, v160, v[176:179]
	v_mfma_f32_16x16x4_f32 v[164:167], v144, v161, v[164:167]
	v_mfma_f32_16x16x4_f32 v[168:171], v145, v161, v[168:171]
	v_mfma_f32_16x16x4_f32 v[172:175], v146, v161, v[172:175]
	v_mfma_f32_16x16x4_f32 v[176:179], v147, v161, v[176:179]
	v_and_b32_e32 v121, 3, v111
	v_and_b32_e32 v122, 8, v111
	v_lshrrev_b32_e32 v122, 1, v122
	v_and_b32_e32 v123, 4, v111
	v_lshlrev_b32_e32 v123, 2, v123
	v_or3_b32 v121, v121, v122, v123
	s_and_b32 s18, s76, 1
	s_lshl_b32 s18, s18, 3
	s_lshr_b32 s19, s76, 1
	s_lshl_b32 s19, s19, 5
	s_or_b32 s18, s18, s19
	v_or_b32_e32 v121, s18, v121
	s_lshl_b32 s18, s43, 18
	s_add_i32 s18, s18, s42
	s_add_i32 s18, s18, 0xe00000
	v_lshlrev_b32_e32 v121, 11, v121
	v_lshl_add_u32 v121, v112, 2, v121
	v_add_u32_e32 v121, s18, v121
	s_nop 15
	v_mul_f32_e32 v124, 0x3db504f3, v164
	v_mul_f32_e32 v125, 0x3db504f3, v165
	v_mul_f32_e32 v126, 0x3db504f3, v166
	v_mul_f32_e32 v127, 0x3db504f3, v167
	v_med3_f32 v124, v124, s61, v54
	v_med3_f32 v125, v125, s61, v54
	v_med3_f32 v126, v126, s61, v54
	v_med3_f32 v127, v127, s61, v54
	v_mov_b32_e32 v128, 0
	v_cvt_pk_fp8_f32 v128, v124, v125
	s_nop 0
	v_cvt_pk_fp8_f32 v128, v126, v127 op_sel:[0,0,1]
	v_mul_f32_e32 v124, 0x3db504f3, v168
	v_mul_f32_e32 v125, 0x3db504f3, v169
	v_mul_f32_e32 v126, 0x3db504f3, v170
	v_mul_f32_e32 v127, 0x3db504f3, v171
	v_med3_f32 v124, v124, s61, v54
	v_med3_f32 v125, v125, s61, v54
	v_med3_f32 v126, v126, s61, v54
	v_med3_f32 v127, v127, s61, v54
	v_mov_b32_e32 v129, 0
	v_cvt_pk_fp8_f32 v129, v124, v125
	s_nop 0
	v_cvt_pk_fp8_f32 v129, v126, v127 op_sel:[0,0,1]
	v_mul_f32_e32 v124, 0x3db504f3, v172
	v_mul_f32_e32 v125, 0x3db504f3, v173
	v_mul_f32_e32 v126, 0x3db504f3, v174
	v_mul_f32_e32 v127, 0x3db504f3, v175
	v_med3_f32 v124, v124, s61, v54
	v_med3_f32 v125, v125, s61, v54
	v_med3_f32 v126, v126, s61, v54
	v_med3_f32 v127, v127, s61, v54
	v_mov_b32_e32 v130, 0
	v_cvt_pk_fp8_f32 v130, v124, v125
	s_nop 0
	v_cvt_pk_fp8_f32 v130, v126, v127 op_sel:[0,0,1]
	v_mul_f32_e32 v124, 0x3db504f3, v176
	v_mul_f32_e32 v125, 0x3db504f3, v177
	v_mul_f32_e32 v126, 0x3db504f3, v178
	v_mul_f32_e32 v127, 0x3db504f3, v179
	v_med3_f32 v124, v124, s61, v54
	v_med3_f32 v125, v125, s61, v54
	v_med3_f32 v126, v126, s61, v54
	v_med3_f32 v127, v127, s61, v54
	v_mov_b32_e32 v131, 0
	v_cvt_pk_fp8_f32 v131, v124, v125
	s_nop 0
	v_cvt_pk_fp8_f32 v131, v126, v127 op_sel:[0,0,1]
	global_store_dword v121, v128, s[28:29]
	global_store_dword v121, v129, s[28:29] offset:16
	global_store_dword v121, v130, s[28:29] offset:32
	global_store_dword v121, v131, s[28:29] offset:48
	s_add_i32 s62, s62, s33
	s_cmpk_gt_i32 s62, 0xff
	s_cbranch_scc0 .LBB0_30

.LBB0_78:
	s_andn2_b64 vcc, exec, s[6:7]
	s_cbranch_vccnz .LBB0_82
	s_and_b32 s4, s38, 63
	s_lshl_b32 s4, s4, 6
	v_add_u32_e32 v34, s4, v62
	v_add_u32_e32 v36, s4, v63
	v_add_u32_e32 v40, s4, v64
	v_add_u32_e32 v42, s4, v65
	v_add_u32_e32 v44, s4, v66
	v_add_u32_e32 v46, s4, v67
	v_add_u32_e32 v48, s4, v68
	v_add_u32_e32 v50, s4, v69
	v_ashrrev_i32_e32 v35, 31, v34
	v_ashrrev_i32_e32 v37, 31, v36
	v_ashrrev_i32_e32 v41, 31, v40
	v_ashrrev_i32_e32 v43, 31, v42
	v_ashrrev_i32_e32 v45, 31, v44
	v_ashrrev_i32_e32 v47, 31, v46
	v_ashrrev_i32_e32 v49, 31, v48
	v_ashrrev_i32_e32 v51, 31, v50
	v_lshlrev_b64 v[34:35], 13, v[34:35]
	v_lshlrev_b64 v[36:37], 13, v[36:37]
	v_lshlrev_b64 v[40:41], 13, v[40:41]
	v_lshlrev_b64 v[42:43], 13, v[42:43]
	v_lshlrev_b64 v[44:45], 13, v[44:45]
	v_lshlrev_b64 v[46:47], 13, v[46:47]
	v_lshlrev_b64 v[48:49], 13, v[48:49]
	v_lshlrev_b64 v[50:51], 13, v[50:51]
	v_or_b32_e32 v34, s23, v34
	v_or_b32_e32 v36, s23, v36
	v_or_b32_e32 v40, s23, v40
	v_or_b32_e32 v42, s23, v42
	v_or_b32_e32 v44, s23, v44
	v_or_b32_e32 v46, s23, v46
	v_or_b32_e32 v48, s23, v48
	v_or_b32_e32 v50, s23, v50
	v_lshl_add_u64 v[34:35], v[32:33], 0, v[34:35]
	v_lshl_add_u64 v[36:37], v[32:33], 0, v[36:37]
	v_lshl_add_u64 v[40:41], v[32:33], 0, v[40:41]
	v_lshl_add_u64 v[42:43], v[32:33], 0, v[42:43]
	v_lshl_add_u64 v[44:45], v[32:33], 0, v[44:45]
	v_lshl_add_u64 v[46:47], v[32:33], 0, v[46:47]
	v_lshl_add_u64 v[48:49], v[32:33], 0, v[48:49]
	v_lshl_add_u64 v[50:51], v[32:33], 0, v[50:51]
	s_mov_b64 s[6:7], 0
	v_mov_b32_e32 v3, v54
	v_lshl_add_u64 v[74:75], v[50:51], 0, s[6:7]
	v_lshl_add_u64 v[76:77], v[48:49], 0, s[6:7]
	v_lshl_add_u64 v[78:79], v[46:47], 0, s[6:7]
	v_lshl_add_u64 v[80:81], v[44:45], 0, s[6:7]
	v_lshl_add_u64 v[82:83], v[42:43], 0, s[6:7]
	v_lshl_add_u64 v[84:85], v[40:41], 0, s[6:7]
	v_lshl_add_u64 v[86:87], v[36:37], 0, s[6:7]
	v_lshl_add_u64 v[88:89], v[34:35], 0, s[6:7]
	global_load_dword v200, v[74:75], off nt
	global_load_dword v201, v[76:77], off nt
	global_load_dword v202, v[78:79], off nt
	global_load_dword v203, v[80:81], off nt
	global_load_dword v204, v[82:83], off nt
	global_load_dword v205, v[84:85], off nt
	global_load_dword v206, v[86:87], off nt
	global_load_dword v207, v[88:89], off nt
	s_add_u32 s6, s6, 0x20000
	s_addc_u32 s7, s7, 0
	v_lshl_add_u64 v[74:75], v[50:51], 0, s[6:7]
	v_lshl_add_u64 v[76:77], v[48:49], 0, s[6:7]
	v_lshl_add_u64 v[78:79], v[46:47], 0, s[6:7]
	v_lshl_add_u64 v[80:81], v[44:45], 0, s[6:7]
	v_lshl_add_u64 v[82:83], v[42:43], 0, s[6:7]
	v_lshl_add_u64 v[84:85], v[40:41], 0, s[6:7]
	v_lshl_add_u64 v[86:87], v[36:37], 0, s[6:7]
	v_lshl_add_u64 v[88:89], v[34:35], 0, s[6:7]
	global_load_dword v208, v[74:75], off nt
	global_load_dword v209, v[76:77], off nt
	global_load_dword v210, v[78:79], off nt
	global_load_dword v211, v[80:81], off nt
	global_load_dword v212, v[82:83], off nt
	global_load_dword v213, v[84:85], off nt
	global_load_dword v214, v[86:87], off nt
	global_load_dword v215, v[88:89], off nt
	s_add_u32 s6, s6, 0x20000
	s_addc_u32 s7, s7, 0
	v_lshl_add_u64 v[74:75], v[50:51], 0, s[6:7]
	v_lshl_add_u64 v[76:77], v[48:49], 0, s[6:7]
	v_lshl_add_u64 v[78:79], v[46:47], 0, s[6:7]
	v_lshl_add_u64 v[80:81], v[44:45], 0, s[6:7]
	v_lshl_add_u64 v[82:83], v[42:43], 0, s[6:7]
	v_lshl_add_u64 v[84:85], v[40:41], 0, s[6:7]
	v_lshl_add_u64 v[86:87], v[36:37], 0, s[6:7]
	v_lshl_add_u64 v[88:89], v[34:35], 0, s[6:7]
	global_load_dword v216, v[74:75], off nt
	global_load_dword v217, v[76:77], off nt
	global_load_dword v218, v[78:79], off nt
	global_load_dword v219, v[80:81], off nt
	global_load_dword v220, v[82:83], off nt
	global_load_dword v221, v[84:85], off nt
	global_load_dword v222, v[86:87], off nt
	global_load_dword v223, v[88:89], off nt
	s_add_u32 s6, s6, 0x20000
	s_addc_u32 s7, s7, 0
	v_lshl_add_u64 v[74:75], v[50:51], 0, s[6:7]
	v_lshl_add_u64 v[76:77], v[48:49], 0, s[6:7]
	v_lshl_add_u64 v[78:79], v[46:47], 0, s[6:7]
	v_lshl_add_u64 v[80:81], v[44:45], 0, s[6:7]
	v_lshl_add_u64 v[82:83], v[42:43], 0, s[6:7]
	v_lshl_add_u64 v[84:85], v[40:41], 0, s[6:7]
	v_lshl_add_u64 v[86:87], v[36:37], 0, s[6:7]
	v_lshl_add_u64 v[88:89], v[34:35], 0, s[6:7]
	global_load_dword v224, v[74:75], off nt
	global_load_dword v225, v[76:77], off nt
	global_load_dword v226, v[78:79], off nt
	global_load_dword v227, v[80:81], off nt
	global_load_dword v228, v[82:83], off nt
	global_load_dword v229, v[84:85], off nt
	global_load_dword v230, v[86:87], off nt
	global_load_dword v231, v[88:89], off nt
	s_add_u32 s6, s6, 0x20000
	s_addc_u32 s7, s7, 0
	v_add_u32_e32 v74, 0x400, v3
	s_waitcnt vmcnt(30)
	ds_write2_b32 v3, v200, v201 offset1:66
	s_waitcnt vmcnt(28)
	ds_write2_b32 v3, v202, v203 offset0:132 offset1:198
	s_waitcnt vmcnt(26)
	ds_write2_b32 v74, v204, v205 offset0:8 offset1:74
	s_waitcnt vmcnt(24)
	ds_write2_b32 v74, v206, v207 offset0:140 offset1:206
	v_add_u32_e32 v3, 0x840, v3
	v_add_u32_e32 v74, 0x400, v3
	s_waitcnt vmcnt(22)
	ds_write2_b32 v3, v208, v209 offset1:66
	s_waitcnt vmcnt(20)
	ds_write2_b32 v3, v210, v211 offset0:132 offset1:198
	s_waitcnt vmcnt(18)
	ds_write2_b32 v74, v212, v213 offset0:8 offset1:74
	s_waitcnt vmcnt(16)
	ds_write2_b32 v74, v214, v215 offset0:140 offset1:206
	v_add_u32_e32 v3, 0x840, v3
	v_add_u32_e32 v74, 0x400, v3
	s_waitcnt vmcnt(14)
	ds_write2_b32 v3, v216, v217 offset1:66
	s_waitcnt vmcnt(12)
	ds_write2_b32 v3, v218, v219 offset0:132 offset1:198
	s_waitcnt vmcnt(10)
	ds_write2_b32 v74, v220, v221 offset0:8 offset1:74
	s_waitcnt vmcnt(8)
	ds_write2_b32 v74, v222, v223 offset0:140 offset1:206
	v_add_u32_e32 v3, 0x840, v3
	v_add_u32_e32 v74, 0x400, v3
	s_waitcnt vmcnt(6)
	ds_write2_b32 v3, v224, v225 offset1:66
	s_waitcnt vmcnt(4)
	ds_write2_b32 v3, v226, v227 offset0:132 offset1:198
	s_waitcnt vmcnt(2)
	ds_write2_b32 v74, v228, v229 offset0:8 offset1:74
	s_waitcnt vmcnt(0)
	ds_write2_b32 v74, v230, v231 offset0:140 offset1:206
	v_add_u32_e32 v3, 0x840, v3
	s_waitcnt lgkmcnt(0)
	ds_read2_b32 v[34:35], v23 offset1:8
	ds_read2_b32 v[36:37], v23 offset0:33 offset1:41
	ds_read2_b32 v[40:41], v23 offset0:66 offset1:74
	ds_read2_b32 v[42:43], v23 offset0:99 offset1:107
	v_mov_b32_e32 v46, v11
	s_waitcnt lgkmcnt(3)
	v_mul_f32_e32 v3, 0x42800000, v34
	s_waitcnt lgkmcnt(2)
	v_mul_f32_e32 v10, 0x42800000, v36
	v_med3_f32 v3, v3, s20, v71
	v_med3_f32 v10, v10, s20, v71
	v_cvt_pk_fp8_f32 v46, v3, v10
	ds_read2_b32 v[48:49], v23 offset0:132 offset1:140
	ds_read2_b32 v[50:51], v23 offset0:165 offset1:173
	ds_read2_b32 v[74:75], v23 offset0:198 offset1:206
	s_waitcnt lgkmcnt(4)
	v_mul_f32_e32 v34, 0x42800000, v40
	s_waitcnt lgkmcnt(3)
	v_mul_f32_e32 v36, 0x42800000, v42
	v_med3_f32 v34, v34, s20, v71
	v_med3_f32 v3, v36, s20, v71
	ds_read2_b32 v[76:77], v23 offset0:231 offset1:239
	v_cvt_pk_fp8_f32 v46, v34, v3 op_sel:[0,0,1]
	s_waitcnt lgkmcnt(3)
	v_mul_f32_e32 v3, 0x42800000, v48
	s_waitcnt lgkmcnt(2)
	v_mul_f32_e32 v10, 0x42800000, v50
	v_med3_f32 v3, v3, s20, v71
	v_med3_f32 v10, v10, s20, v71
	v_mov_b32_e32 v47, v11
	v_cvt_pk_fp8_f32 v47, v3, v10
	s_lshl_b32 s6, s22, 5
	s_waitcnt lgkmcnt(1)
	v_mul_f32_e32 v34, 0x42800000, v74
	s_waitcnt lgkmcnt(0)
	v_mul_f32_e32 v3, 0x42800000, v76
	s_and_b32 s4, s22, 0xfc0
	s_and_b32 s6, s6, 0x7e0
	v_med3_f32 v10, v34, s20, v71
	v_med3_f32 v3, v3, s20, v71
	s_addk_i32 s4, 0xf800
	v_cvt_pk_fp8_f32 v47, v10, v3 op_sel:[0,0,1]
	v_or_b32_e32 v3, s6, v18
	v_lshl_add_u64 v[44:45], v[20:21], 0, s[4:5]
	v_lshlrev_b32_e32 v10, 11, v3
	v_lshl_add_u64 v[78:79], v[44:45], 0, v[10:11]
	v_mul_f32_e32 v3, 0x42800000, v35
	v_mul_f32_e32 v10, 0x42800000, v37
	v_med3_f32 v3, v3, s20, v71
	v_med3_f32 v10, v10, s20, v71
	v_mov_b32_e32 v34, v11
	v_cvt_pk_fp8_f32 v34, v3, v10
	v_mul_f32_e32 v35, 0x42800000, v41
	v_mul_f32_e32 v3, 0x42800000, v43
	v_med3_f32 v10, v35, s20, v71
	v_med3_f32 v3, v3, s20, v71
	v_cvt_pk_fp8_f32 v34, v10, v3 op_sel:[0,0,1]
	v_mul_f32_e32 v3, 0x42800000, v49
	v_mul_f32_e32 v10, 0x42800000, v51
	v_med3_f32 v3, v3, s20, v71
	v_med3_f32 v10, v10, s20, v71
	v_mov_b32_e32 v35, v11
	v_cvt_pk_fp8_f32 v35, v3, v10
	v_mul_f32_e32 v36, 0x42800000, v75
	v_mul_f32_e32 v3, 0x42800000, v77
	global_store_dwordx2 v[78:79], v[46:47], off
	v_med3_f32 v10, v36, s20, v71
	v_med3_f32 v3, v3, s20, v71
	v_cvt_pk_fp8_f32 v35, v10, v3 op_sel:[0,0,1]
	ds_read2_b32 v[40:41], v23 offset0:16 offset1:24
	ds_read2_b32 v[42:43], v23 offset0:49 offset1:57
	ds_read2_b32 v[46:47], v23 offset0:82 offset1:90
	ds_read2_b32 v[48:49], v23 offset0:115 offset1:123
	v_or_b32_e32 v3, s6, v22
	v_lshlrev_b32_e32 v10, 11, v3
	v_lshl_add_u64 v[36:37], v[44:45], 0, v[10:11]
	global_store_dwordx2 v[36:37], v[34:35], off
	s_waitcnt lgkmcnt(3)
	v_mul_f32_e32 v3, 0x42800000, v40
	s_waitcnt lgkmcnt(2)
	v_mul_f32_e32 v10, 0x42800000, v42
	s_waitcnt lgkmcnt(1)
	v_mul_f32_e32 v34, 0x42800000, v46
	v_med3_f32 v3, v3, s20, v71
	v_med3_f32 v10, v10, s20, v71
	v_med3_f32 v40, v34, s20, v71
	v_mov_b32_e32 v34, v11
	v_cvt_pk_fp8_f32 v34, v3, v10
	ds_read2_b32 v[36:37], v23 offset0:148 offset1:156
	ds_read2_b32 v[50:51], v23 offset0:181 offset1:189
	ds_read2_b32 v[74:75], v23 offset0:214 offset1:222
	s_waitcnt lgkmcnt(3)
	v_mul_f32_e32 v35, 0x42800000, v48
	v_med3_f32 v3, v35, s20, v71
	ds_read2_b32 v[76:77], v23 offset0:247 offset1:255
	v_cvt_pk_fp8_f32 v34, v40, v3 op_sel:[0,0,1]
	s_waitcnt lgkmcnt(3)
	v_mul_f32_e32 v3, 0x42800000, v36
	s_waitcnt lgkmcnt(2)
	v_mul_f32_e32 v10, 0x42800000, v50
	v_med3_f32 v3, v3, s20, v71
	v_med3_f32 v10, v10, s20, v71
	v_mov_b32_e32 v35, v11
	v_cvt_pk_fp8_f32 v35, v3, v10
	s_waitcnt lgkmcnt(1)
	v_mul_f32_e32 v36, 0x42800000, v74
	s_waitcnt lgkmcnt(0)
	v_mul_f32_e32 v3, 0x42800000, v76
	v_med3_f32 v10, v36, s20, v71
	v_med3_f32 v3, v3, s20, v71
	v_cvt_pk_fp8_f32 v35, v10, v3 op_sel:[0,0,1]
	v_or_b32_e32 v3, s6, v24
	v_lshlrev_b32_e32 v10, 11, v3
	v_lshl_add_u64 v[78:79], v[44:45], 0, v[10:11]
	global_store_dwordx2 v[78:79], v[34:35], off
	v_mul_f32_e32 v10, 0x42800000, v41
	v_mul_f32_e32 v34, 0x42800000, v43
	v_med3_f32 v10, v10, s20, v71
	v_med3_f32 v35, v34, s20, v71
	v_mov_b32_e32 v34, v11
	v_cvt_pk_fp8_f32 v34, v10, v35
	v_mul_f32_e32 v3, 0x42800000, v47
	v_mul_f32_e32 v10, 0x42800000, v49
	v_med3_f32 v3, v3, s20, v71
	v_med3_f32 v10, v10, s20, v71
	v_cvt_pk_fp8_f32 v34, v3, v10 op_sel:[0,0,1]
	v_mul_f32_e32 v10, 0x42800000, v37
	v_mul_f32_e32 v35, 0x42800000, v51
	v_med3_f32 v10, v10, s20, v71
	v_med3_f32 v36, v35, s20, v71
	v_mov_b32_e32 v35, v11
	v_cvt_pk_fp8_f32 v35, v10, v36
	v_mul_f32_e32 v3, 0x42800000, v75
	v_mul_f32_e32 v10, 0x42800000, v77
	v_med3_f32 v3, v3, s20, v71
	v_med3_f32 v10, v10, s20, v71
	v_cvt_pk_fp8_f32 v35, v3, v10 op_sel:[0,0,1]
	v_or_b32_e32 v3, s6, v26
	v_lshlrev_b32_e32 v10, 11, v3
	v_lshl_add_u64 v[36:37], v[44:45], 0, v[10:11]
	global_store_dwordx2 v[36:37], v[34:35], off
	s_waitcnt lgkmcnt(0)

.LBB0_83:
	s_andn2_b64 vcc, exec, s[6:7]
	s_cbranch_vccnz .LBB0_56
	s_ashr_i32 s4, s22, 31
	s_lshr_b32 s4, s4, 26
	s_add_i32 s4, s22, s4
	s_and_b32 s8, s4, 0xffffffc0
	s_sub_i32 s6, s22, s8
	s_lshl_b32 s10, s6, 5
	s_ashr_i32 s11, s10, 31
	v_lshl_add_u64 v[34:35], s[10:11], 2, v[30:31]
	v_or_b32_e32 v3, s8, v4
	s_mov_b32 s4, 0
	v_mov_b32_e32 v10, v54
	v_mov_b32_e32 v40, v3
	v_mad_i64_i32 v[36:37], s[10:11], v40, s21, v[34:35]
	v_add_u32_e32 v41, 2, v40
	v_add_u32_e32 v42, 4, v40
	v_add_u32_e32 v44, 6, v40
	v_add_u32_e32 v46, 8, v40
	v_add_u32_e32 v48, 10, v40
	v_add_u32_e32 v50, 12, v40
	v_add_u32_e32 v74, 14, v40
	v_mad_i64_i32 v[40:41], s[10:11], v41, s21, v[34:35]
	v_mad_i64_i32 v[42:43], s[10:11], v42, s21, v[34:35]
	v_mad_i64_i32 v[44:45], s[10:11], v44, s21, v[34:35]
	v_mad_i64_i32 v[46:47], s[10:11], v46, s21, v[34:35]
	v_mad_i64_i32 v[48:49], s[10:11], v48, s21, v[34:35]
	v_mad_i64_i32 v[50:51], s[10:11], v50, s21, v[34:35]
	v_mad_i64_i32 v[74:75], s[10:11], v74, s21, v[34:35]
	global_load_dword v200, v[36:37], off nt
	global_load_dword v201, v[40:41], off nt
	global_load_dword v202, v[42:43], off nt
	global_load_dword v203, v[44:45], off nt
	global_load_dword v204, v[46:47], off nt
	global_load_dword v205, v[48:49], off nt
	global_load_dword v206, v[50:51], off nt
	global_load_dword v207, v[74:75], off nt
	v_add_u32_e32 v40, 16, v3
	v_mad_i64_i32 v[36:37], s[10:11], v40, s21, v[34:35]
	v_add_u32_e32 v41, 2, v40
	v_add_u32_e32 v42, 4, v40
	v_add_u32_e32 v44, 6, v40
	v_add_u32_e32 v46, 8, v40
	v_add_u32_e32 v48, 10, v40
	v_add_u32_e32 v50, 12, v40
	v_add_u32_e32 v74, 14, v40
	v_mad_i64_i32 v[40:41], s[10:11], v41, s21, v[34:35]
	v_mad_i64_i32 v[42:43], s[10:11], v42, s21, v[34:35]
	v_mad_i64_i32 v[44:45], s[10:11], v44, s21, v[34:35]
	v_mad_i64_i32 v[46:47], s[10:11], v46, s21, v[34:35]
	v_mad_i64_i32 v[48:49], s[10:11], v48, s21, v[34:35]
	v_mad_i64_i32 v[50:51], s[10:11], v50, s21, v[34:35]
	v_mad_i64_i32 v[74:75], s[10:11], v74, s21, v[34:35]
	global_load_dword v208, v[36:37], off nt
	global_load_dword v209, v[40:41], off nt
	global_load_dword v210, v[42:43], off nt
	global_load_dword v211, v[44:45], off nt
	global_load_dword v212, v[46:47], off nt
	global_load_dword v213, v[48:49], off nt
	global_load_dword v214, v[50:51], off nt
	global_load_dword v215, v[74:75], off nt
	v_add_u32_e32 v40, 32, v3
	v_mad_i64_i32 v[36:37], s[10:11], v40, s21, v[34:35]
	v_add_u32_e32 v41, 2, v40
	v_add_u32_e32 v42, 4, v40
	v_add_u32_e32 v44, 6, v40
	v_add_u32_e32 v46, 8, v40
	v_add_u32_e32 v48, 10, v40
	v_add_u32_e32 v50, 12, v40
	v_add_u32_e32 v74, 14, v40
	v_mad_i64_i32 v[40:41], s[10:11], v41, s21, v[34:35]
	v_mad_i64_i32 v[42:43], s[10:11], v42, s21, v[34:35]
	v_mad_i64_i32 v[44:45], s[10:11], v44, s21, v[34:35]
	v_mad_i64_i32 v[46:47], s[10:11], v46, s21, v[34:35]
	v_mad_i64_i32 v[48:49], s[10:11], v48, s21, v[34:35]
	v_mad_i64_i32 v[50:51], s[10:11], v50, s21, v[34:35]
	v_mad_i64_i32 v[74:75], s[10:11], v74, s21, v[34:35]
	global_load_dword v216, v[36:37], off nt
	global_load_dword v217, v[40:41], off nt
	global_load_dword v218, v[42:43], off nt
	global_load_dword v219, v[44:45], off nt
	global_load_dword v220, v[46:47], off nt
	global_load_dword v221, v[48:49], off nt
	global_load_dword v222, v[50:51], off nt
	global_load_dword v223, v[74:75], off nt
	v_add_u32_e32 v40, 48, v3
	v_mad_i64_i32 v[36:37], s[10:11], v40, s21, v[34:35]
	v_add_u32_e32 v41, 2, v40
	v_add_u32_e32 v42, 4, v40
	v_add_u32_e32 v44, 6, v40
	v_add_u32_e32 v46, 8, v40
	v_add_u32_e32 v48, 10, v40
	v_add_u32_e32 v50, 12, v40
	v_add_u32_e32 v74, 14, v40
	v_mad_i64_i32 v[40:41], s[10:11], v41, s21, v[34:35]
	v_mad_i64_i32 v[42:43], s[10:11], v42, s21, v[34:35]
	v_mad_i64_i32 v[44:45], s[10:11], v44, s21, v[34:35]
	v_mad_i64_i32 v[46:47], s[10:11], v46, s21, v[34:35]
	v_mad_i64_i32 v[48:49], s[10:11], v48, s21, v[34:35]
	v_mad_i64_i32 v[50:51], s[10:11], v50, s21, v[34:35]
	v_mad_i64_i32 v[74:75], s[10:11], v74, s21, v[34:35]
	global_load_dword v224, v[36:37], off nt
	global_load_dword v225, v[40:41], off nt
	global_load_dword v226, v[42:43], off nt
	global_load_dword v227, v[44:45], off nt
	global_load_dword v228, v[46:47], off nt
	global_load_dword v229, v[48:49], off nt
	global_load_dword v230, v[50:51], off nt
	global_load_dword v231, v[74:75], off nt
	v_add_u32_e32 v36, 0x400, v10
	s_waitcnt vmcnt(30)
	ds_write2_b32 v10, v200, v201 offset1:66
	s_waitcnt vmcnt(28)
	ds_write2_b32 v10, v202, v203 offset0:132 offset1:198
	s_waitcnt vmcnt(26)
	ds_write2_b32 v36, v204, v205 offset0:8 offset1:74
	s_waitcnt vmcnt(24)
	ds_write2_b32 v36, v206, v207 offset0:140 offset1:206
	v_add_u32_e32 v10, 0x840, v10
	v_add_u32_e32 v36, 0x400, v10
	s_waitcnt vmcnt(22)
	ds_write2_b32 v10, v208, v209 offset1:66
	s_waitcnt vmcnt(20)
	ds_write2_b32 v10, v210, v211 offset0:132 offset1:198
	s_waitcnt vmcnt(18)
	ds_write2_b32 v36, v212, v213 offset0:8 offset1:74
	s_waitcnt vmcnt(16)
	ds_write2_b32 v36, v214, v215 offset0:140 offset1:206
	v_add_u32_e32 v10, 0x840, v10
	v_add_u32_e32 v36, 0x400, v10
	s_waitcnt vmcnt(14)
	ds_write2_b32 v10, v216, v217 offset1:66
	s_waitcnt vmcnt(12)
	ds_write2_b32 v10, v218, v219 offset0:132 offset1:198
	s_waitcnt vmcnt(10)
	ds_write2_b32 v36, v220, v221 offset0:8 offset1:74
	s_waitcnt vmcnt(8)
	ds_write2_b32 v36, v222, v223 offset0:140 offset1:206
	v_add_u32_e32 v10, 0x840, v10
	v_add_u32_e32 v36, 0x400, v10
	s_waitcnt vmcnt(6)
	ds_write2_b32 v10, v224, v225 offset1:66
	s_waitcnt vmcnt(4)
	ds_write2_b32 v10, v226, v227 offset0:132 offset1:198
	s_waitcnt vmcnt(2)
	ds_write2_b32 v36, v228, v229 offset0:8 offset1:74
	s_waitcnt vmcnt(0)
	ds_write2_b32 v36, v230, v231 offset0:140 offset1:206
	v_add_u32_e32 v10, 0x840, v10
	s_waitcnt lgkmcnt(0)
	ds_read2_b32 v[34:35], v23 offset1:8
	ds_read2_b32 v[36:37], v23 offset0:33 offset1:41
	ds_read2_b32 v[40:41], v23 offset0:66 offset1:74
	ds_read2_b32 v[42:43], v23 offset0:99 offset1:107
	v_mov_b32_e32 v46, v11
	s_waitcnt lgkmcnt(3)
	v_mul_f32_e32 v3, 0x42800000, v34
	s_waitcnt lgkmcnt(2)
	v_mul_f32_e32 v10, 0x42800000, v36
	v_med3_f32 v3, v3, s20, v71
	v_med3_f32 v10, v10, s20, v71
	v_cvt_pk_fp8_f32 v46, v3, v10
	ds_read2_b32 v[48:49], v23 offset0:132 offset1:140
	ds_read2_b32 v[50:51], v23 offset0:165 offset1:173
	ds_read2_b32 v[74:75], v23 offset0:198 offset1:206
	s_waitcnt lgkmcnt(4)
	v_mul_f32_e32 v34, 0x42800000, v40
	s_waitcnt lgkmcnt(3)
	v_mul_f32_e32 v36, 0x42800000, v42
	v_med3_f32 v34, v34, s20, v71
	v_med3_f32 v3, v36, s20, v71
	ds_read2_b32 v[76:77], v23 offset0:231 offset1:239
	v_cvt_pk_fp8_f32 v46, v34, v3 op_sel:[0,0,1]
	s_waitcnt lgkmcnt(3)
	v_mul_f32_e32 v3, 0x42800000, v48
	s_waitcnt lgkmcnt(2)
	v_mul_f32_e32 v10, 0x42800000, v50
	v_med3_f32 v3, v3, s20, v71
	v_med3_f32 v10, v10, s20, v71
	v_mov_b32_e32 v47, v11
	v_cvt_pk_fp8_f32 v47, v3, v10
	s_waitcnt lgkmcnt(1)
	v_mul_f32_e32 v34, 0x42800000, v74
	s_waitcnt lgkmcnt(0)
	v_mul_f32_e32 v3, 0x42800000, v76
	v_med3_f32 v10, v34, s20, v71
	v_med3_f32 v3, v3, s20, v71
	v_cvt_pk_fp8_f32 v47, v10, v3 op_sel:[0,0,1]
	v_mul_f32_e32 v3, 0x42800000, v35
	v_mul_f32_e32 v10, 0x42800000, v37
	v_med3_f32 v3, v3, s20, v71
	v_med3_f32 v10, v10, s20, v71
	v_mov_b32_e32 v34, v11
	v_cvt_pk_fp8_f32 v34, v3, v10
	v_mul_f32_e32 v35, 0x42800000, v41
	v_mul_f32_e32 v3, 0x42800000, v43
	v_med3_f32 v10, v35, s20, v71
	v_med3_f32 v3, v3, s20, v71
	s_ashr_i32 s7, s6, 31
	v_cvt_pk_fp8_f32 v34, v10, v3 op_sel:[0,0,1]
	v_mul_f32_e32 v3, 0x42800000, v49
	v_mul_f32_e32 v10, 0x42800000, v51
	s_lshl_b64 s[6:7], s[6:7], 5
	v_med3_f32 v3, v3, s20, v71
	v_med3_f32 v10, v10, s20, v71
	v_mov_b32_e32 v35, v11
	s_ashr_i32 s9, s8, 31
	v_mov_b32_e32 v79, s7
	v_or_b32_e32 v78, s6, v18
	v_cvt_pk_fp8_f32 v35, v3, v10
	v_lshl_add_u64 v[44:45], v[28:29], 0, s[8:9]
	v_lshlrev_b64 v[78:79], 11, v[78:79]
	v_lshl_add_u64 v[78:79], v[44:45], 0, v[78:79]
	v_mul_f32_e32 v36, 0x42800000, v75
	v_mul_f32_e32 v3, 0x42800000, v77
	global_store_dwordx2 v[78:79], v[46:47], off
	v_med3_f32 v10, v36, s20, v71
	v_med3_f32 v3, v3, s20, v71
	v_cvt_pk_fp8_f32 v35, v10, v3 op_sel:[0,0,1]
	ds_read2_b32 v[40:41], v23 offset0:16 offset1:24
	ds_read2_b32 v[42:43], v23 offset0:49 offset1:57
	ds_read2_b32 v[46:47], v23 offset0:82 offset1:90
	ds_read2_b32 v[48:49], v23 offset0:115 offset1:123
	v_mov_b32_e32 v37, s7
	v_or_b32_e32 v36, s6, v22
	v_lshlrev_b64 v[36:37], 11, v[36:37]
	v_lshl_add_u64 v[36:37], v[44:45], 0, v[36:37]
	global_store_dwordx2 v[36:37], v[34:35], off
	s_waitcnt lgkmcnt(3)
	v_mul_f32_e32 v3, 0x42800000, v40
	s_waitcnt lgkmcnt(2)
	v_mul_f32_e32 v10, 0x42800000, v42
	s_waitcnt lgkmcnt(1)
	v_mul_f32_e32 v34, 0x42800000, v46
	v_med3_f32 v3, v3, s20, v71
	v_med3_f32 v10, v10, s20, v71
	v_med3_f32 v40, v34, s20, v71
	v_mov_b32_e32 v34, v11
	v_cvt_pk_fp8_f32 v34, v3, v10
	ds_read2_b32 v[36:37], v23 offset0:148 offset1:156
	ds_read2_b32 v[50:51], v23 offset0:181 offset1:189
	ds_read2_b32 v[74:75], v23 offset0:214 offset1:222
	s_waitcnt lgkmcnt(3)
	v_mul_f32_e32 v35, 0x42800000, v48
	v_med3_f32 v3, v35, s20, v71
	ds_read2_b32 v[76:77], v23 offset0:247 offset1:255
	v_cvt_pk_fp8_f32 v34, v40, v3 op_sel:[0,0,1]
	s_waitcnt lgkmcnt(3)
	v_mul_f32_e32 v3, 0x42800000, v36
	s_waitcnt lgkmcnt(2)
	v_mul_f32_e32 v10, 0x42800000, v50
	v_med3_f32 v3, v3, s20, v71
	v_med3_f32 v10, v10, s20, v71
	v_mov_b32_e32 v35, v11
	v_cvt_pk_fp8_f32 v35, v3, v10
	s_waitcnt lgkmcnt(1)
	v_mul_f32_e32 v36, 0x42800000, v74
	s_waitcnt lgkmcnt(0)
	v_mul_f32_e32 v3, 0x42800000, v76
	v_med3_f32 v10, v36, s20, v71
	v_med3_f32 v3, v3, s20, v71
	v_cvt_pk_fp8_f32 v35, v10, v3 op_sel:[0,0,1]
	v_mov_b32_e32 v79, s7
	v_or_b32_e32 v78, s6, v24
	v_lshlrev_b64 v[78:79], 11, v[78:79]
	v_lshl_add_u64 v[78:79], v[44:45], 0, v[78:79]
	global_store_dwordx2 v[78:79], v[34:35], off
	v_mul_f32_e32 v10, 0x42800000, v41
	v_mul_f32_e32 v34, 0x42800000, v43
	v_med3_f32 v10, v10, s20, v71
	v_med3_f32 v35, v34, s20, v71
	v_mov_b32_e32 v34, v11
	v_cvt_pk_fp8_f32 v34, v10, v35
	v_mul_f32_e32 v3, 0x42800000, v47
	v_mul_f32_e32 v10, 0x42800000, v49
	v_med3_f32 v3, v3, s20, v71
	v_med3_f32 v10, v10, s20, v71
	v_cvt_pk_fp8_f32 v34, v3, v10 op_sel:[0,0,1]
	v_mul_f32_e32 v10, 0x42800000, v37
	v_mul_f32_e32 v35, 0x42800000, v51
	v_med3_f32 v10, v10, s20, v71
	v_med3_f32 v36, v35, s20, v71
	v_mov_b32_e32 v35, v11
	v_cvt_pk_fp8_f32 v35, v10, v36
	v_mul_f32_e32 v3, 0x42800000, v75
	v_mul_f32_e32 v10, 0x42800000, v77
	v_med3_f32 v3, v3, s20, v71
	v_med3_f32 v10, v10, s20, v71
	v_cvt_pk_fp8_f32 v35, v3, v10 op_sel:[0,0,1]
	v_mov_b32_e32 v37, s7
	v_or_b32_e32 v36, s6, v26
	v_lshlrev_b64 v[36:37], 11, v[36:37]
	v_lshl_add_u64 v[36:37], v[44:45], 0, v[36:37]
	global_store_dwordx2 v[36:37], v[34:35], off
	s_waitcnt lgkmcnt(0)
	s_branch .LBB0_56
